# speedup vs baseline: 1.0419x; 1.0043x over previous
.LBB5_5:
	s_load_dwordx2 s[62:63], s[0:1], 0x20
	s_load_dwordx2 s[64:65], s[0:1], 0x50
	v_mov_b32_e32 v33, 0
	s_andn2_b64 vcc, exec, s[6:7]
	v_mov_b32_e32 v32, v33
	v_mov_b32_e32 v31, v33
	v_mov_b32_e32 v30, v33
	v_mov_b32_e32 v29, v33
	v_mov_b32_e32 v28, v33
	v_mov_b32_e32 v27, v33
	v_mov_b32_e32 v26, v33
	v_mov_b32_e32 v65, v33
	v_mov_b32_e32 v64, v33
	v_mov_b32_e32 v63, v33
	v_mov_b32_e32 v62, v33
	v_mov_b32_e32 v61, v33
	v_mov_b32_e32 v60, v33
	v_mov_b32_e32 v59, v33
	v_mov_b32_e32 v58, v33
	v_mov_b32_e32 v9, v33
	v_mov_b32_e32 v8, v33
	v_mov_b32_e32 v7, v33
	v_mov_b32_e32 v6, v33
	v_mov_b32_e32 v5, v33
	v_mov_b32_e32 v4, v33
	v_mov_b32_e32 v3, v33
	v_mov_b32_e32 v2, v33
	v_mov_b32_e32 v73, v33
	v_mov_b32_e32 v72, v33
	v_mov_b32_e32 v71, v33
	v_mov_b32_e32 v70, v33
	v_mov_b32_e32 v69, v33
	v_mov_b32_e32 v68, v33
	v_mov_b32_e32 v67, v33
	v_mov_b32_e32 v66, v33
	v_mov_b32_e32 v17, v33
	v_mov_b32_e32 v16, v33
	v_mov_b32_e32 v15, v33
	v_mov_b32_e32 v14, v33
	v_mov_b32_e32 v13, v33
	v_mov_b32_e32 v12, v33
	v_mov_b32_e32 v11, v33
	v_mov_b32_e32 v10, v33
	v_mov_b32_e32 v81, v33
	v_mov_b32_e32 v80, v33
	v_mov_b32_e32 v79, v33
	v_mov_b32_e32 v78, v33
	v_mov_b32_e32 v77, v33
	v_mov_b32_e32 v76, v33
	v_mov_b32_e32 v75, v33
	v_mov_b32_e32 v74, v33
	v_mov_b32_e32 v25, v33
	v_mov_b32_e32 v24, v33
	v_mov_b32_e32 v23, v33
	v_mov_b32_e32 v22, v33
	v_mov_b32_e32 v21, v33
	v_mov_b32_e32 v20, v33
	v_mov_b32_e32 v19, v33
	v_mov_b32_e32 v18, v33
	v_mov_b32_e32 v89, v33
	v_mov_b32_e32 v88, v33
	v_mov_b32_e32 v87, v33
	v_mov_b32_e32 v86, v33
	v_mov_b32_e32 v85, v33
	v_mov_b32_e32 v84, v33
	v_mov_b32_e32 v83, v33
	v_mov_b32_e32 v82, v33
	v_mov_b32_e32 v41, v33
	v_mov_b32_e32 v40, v33
	v_mov_b32_e32 v39, v33
	v_mov_b32_e32 v38, v33
	v_mov_b32_e32 v37, v33
	v_mov_b32_e32 v36, v33
	v_mov_b32_e32 v35, v33
	v_mov_b32_e32 v34, v33
	v_mov_b32_e32 v97, v33
	v_mov_b32_e32 v96, v33
	v_mov_b32_e32 v95, v33
	v_mov_b32_e32 v94, v33
	v_mov_b32_e32 v93, v33
	v_mov_b32_e32 v92, v33
	v_mov_b32_e32 v91, v33
	v_mov_b32_e32 v90, v33
	v_mov_b32_e32 v49, v33
	v_mov_b32_e32 v48, v33
	v_mov_b32_e32 v47, v33
	v_mov_b32_e32 v46, v33
	v_mov_b32_e32 v45, v33
	v_mov_b32_e32 v44, v33
	v_mov_b32_e32 v43, v33
	v_mov_b32_e32 v42, v33
	v_mov_b32_e32 v105, v33
	v_mov_b32_e32 v104, v33
	v_mov_b32_e32 v103, v33
	v_mov_b32_e32 v102, v33
	v_mov_b32_e32 v101, v33
	v_mov_b32_e32 v100, v33
	v_mov_b32_e32 v99, v33
	v_mov_b32_e32 v98, v33
	v_mov_b32_e32 v57, v33
	v_mov_b32_e32 v56, v33
	v_mov_b32_e32 v55, v33
	v_mov_b32_e32 v54, v33
	v_mov_b32_e32 v53, v33
	v_mov_b32_e32 v52, v33
	v_mov_b32_e32 v51, v33
	v_mov_b32_e32 v50, v33
	v_mov_b32_e32 v113, v33
	v_mov_b32_e32 v112, v33
	v_mov_b32_e32 v111, v33
	v_mov_b32_e32 v110, v33
	v_mov_b32_e32 v109, v33
	v_mov_b32_e32 v108, v33
	v_mov_b32_e32 v107, v33
	v_mov_b32_e32 v106, v33
	v_lshrrev_b32_e32 v138, 4, v136
	s_cbranch_vccnz .LBB5_12
	v_mul_u32_u24_e32 v137, 0x70, v135
	s_ashr_i32 s0, s8, 31
	v_or_b32_e32 v2, v137, v1
	v_lshrrev_b32_e32 v3, 1, v0
	v_bfe_u32 v4, v0, 1, 3
	s_lshr_b32 s0, s0, 26
	v_bitop3_b32 v3, v138, v3, 7 bitop3:0x78
	v_lshlrev_b32_e32 v143, 7, v2
	v_bitop3_b32 v2, v138, v4, 4 bitop3:0x36
	v_add_u32_e32 v106, v126, v132
	v_mov_b32_e32 v107, 0
	s_add_i32 s8, s8, s0
	v_lshlrev_b32_e32 v142, 4, v3
	v_lshlrev_b32_e32 v144, 4, v2
	v_lshl_add_u64 v[2:3], v[106:107], 1, s[52:53]
	s_mov_b64 s[0:1], 0x61a800
	v_add_u32_e32 v106, v128, v132
	v_lshlrev_b32_e32 v140, 13, v127
	v_lshl_add_u64 v[126:127], v[2:3], 0, s[0:1]
	v_lshl_add_u64 v[2:3], v[106:107], 1, s[52:53]
	v_add_u32_e32 v106, v130, v132
	v_lshl_add_u64 v[128:129], v[2:3], 0, s[0:1]
	v_lshl_add_u64 v[2:3], v[106:107], 1, s[52:53]
	v_add_u32_e32 v106, v133, v132
	v_lshl_add_u64 v[130:131], v[2:3], 0, s[0:1]
	v_lshl_add_u64 v[2:3], v[106:107], 1, s[52:53]
	s_mov_b32 s7, 0
	s_ashr_i32 s11, s8, 6
	v_lshlrev_b32_e32 v141, 7, v1
	v_lshl_add_u64 v[132:133], v[2:3], 0, s[0:1]
	s_mov_b32 s6, 64
	s_mov_b32 s12, s7
	v_mov_b32_e32 v106, v107
	v_mov_b32_e32 v108, v107
	v_mov_b32_e32 v109, v107
	v_mov_b32_e32 v110, v107
	v_mov_b32_e32 v111, v107
	v_mov_b32_e32 v112, v107
	v_mov_b32_e32 v113, v107
	v_mov_b32_e32 v50, v107
	v_mov_b32_e32 v51, v107
	v_mov_b32_e32 v52, v107
	v_mov_b32_e32 v53, v107
	v_mov_b32_e32 v54, v107
	v_mov_b32_e32 v55, v107
	v_mov_b32_e32 v56, v107
	v_mov_b32_e32 v57, v107
	v_mov_b32_e32 v98, v107
	v_mov_b32_e32 v99, v107
	v_mov_b32_e32 v100, v107
	v_mov_b32_e32 v101, v107
	v_mov_b32_e32 v102, v107
	v_mov_b32_e32 v103, v107
	v_mov_b32_e32 v104, v107
	v_mov_b32_e32 v105, v107
	v_mov_b32_e32 v42, v107
	v_mov_b32_e32 v43, v107
	v_mov_b32_e32 v44, v107
	v_mov_b32_e32 v45, v107
	v_mov_b32_e32 v46, v107
	v_mov_b32_e32 v47, v107
	v_mov_b32_e32 v48, v107
	v_mov_b32_e32 v49, v107
	v_mov_b32_e32 v90, v107
	v_mov_b32_e32 v91, v107
	v_mov_b32_e32 v92, v107
	v_mov_b32_e32 v93, v107
	v_mov_b32_e32 v94, v107
	v_mov_b32_e32 v95, v107
	v_mov_b32_e32 v96, v107
	v_mov_b32_e32 v97, v107
	v_mov_b32_e32 v34, v107
	v_mov_b32_e32 v35, v107
	v_mov_b32_e32 v36, v107
	v_mov_b32_e32 v37, v107
	v_mov_b32_e32 v38, v107
	v_mov_b32_e32 v39, v107
	v_mov_b32_e32 v40, v107
	v_mov_b32_e32 v41, v107
	v_mov_b32_e32 v82, v107
	v_mov_b32_e32 v83, v107
	v_mov_b32_e32 v84, v107
	v_mov_b32_e32 v85, v107
	v_mov_b32_e32 v86, v107
	v_mov_b32_e32 v87, v107
	v_mov_b32_e32 v88, v107
	v_mov_b32_e32 v89, v107
	v_mov_b32_e32 v18, v107
	v_mov_b32_e32 v19, v107
	v_mov_b32_e32 v20, v107
	v_mov_b32_e32 v21, v107
	v_mov_b32_e32 v22, v107
	v_mov_b32_e32 v23, v107
	v_mov_b32_e32 v24, v107
	v_mov_b32_e32 v25, v107
	v_mov_b32_e32 v74, v107
	v_mov_b32_e32 v75, v107
	v_mov_b32_e32 v76, v107
	v_mov_b32_e32 v77, v107
	v_mov_b32_e32 v78, v107
	v_mov_b32_e32 v79, v107
	v_mov_b32_e32 v80, v107
	v_mov_b32_e32 v81, v107
	v_mov_b32_e32 v10, v107
	v_mov_b32_e32 v11, v107
	v_mov_b32_e32 v12, v107
	v_mov_b32_e32 v13, v107
	v_mov_b32_e32 v14, v107
	v_mov_b32_e32 v15, v107
	v_mov_b32_e32 v16, v107
	v_mov_b32_e32 v17, v107
	v_mov_b32_e32 v66, v107
	v_mov_b32_e32 v67, v107
	v_mov_b32_e32 v68, v107
	v_mov_b32_e32 v69, v107
	v_mov_b32_e32 v70, v107
	v_mov_b32_e32 v71, v107
	v_mov_b32_e32 v72, v107
	v_mov_b32_e32 v73, v107
	v_mov_b32_e32 v2, v107
	v_mov_b32_e32 v3, v107
	v_mov_b32_e32 v4, v107
	v_mov_b32_e32 v5, v107
	v_mov_b32_e32 v6, v107
	v_mov_b32_e32 v7, v107
	v_mov_b32_e32 v8, v107
	v_mov_b32_e32 v9, v107
	v_mov_b32_e32 v58, v107
	v_mov_b32_e32 v59, v107
	v_mov_b32_e32 v60, v107
	v_mov_b32_e32 v61, v107
	v_mov_b32_e32 v62, v107
	v_mov_b32_e32 v63, v107
	v_mov_b32_e32 v64, v107
	v_mov_b32_e32 v65, v107
	v_mov_b32_e32 v26, v107
	v_mov_b32_e32 v27, v107
	v_mov_b32_e32 v28, v107
	v_mov_b32_e32 v29, v107
	v_mov_b32_e32 v30, v107
	v_mov_b32_e32 v31, v107
	v_mov_b32_e32 v32, v107
	v_mov_b32_e32 v33, v107
	v_readfirstlane_b32 s75, v139
	s_cmp_lg_u64 s[4:5], 0
	s_cselect_b32 s92, 1, 0
	s_mov_b32 s72, 0x80
	s_mov_b32 s73, 0
	s_add_u32 s8, s54, 0x80
	s_addc_u32 s9, s55, 0
	s_add_i32 s76, s75, 0x0
	s_add_i32 s77, s75, 0x2000
	s_add_i32 s78, s75, 0x4000
	s_add_i32 s79, s75, 0x6000
	s_add_i32 s80, s75, 0x7000
	s_add_i32 s81, s75, 0x9000
	s_add_i32 s82, s75, 0xb000
	s_add_i32 s83, s75, 0xd000
	s_add_i32 s84, s75, 0xf000
	s_add_i32 s85, s75, 0x11000
	s_add_i32 s86, s75, 0x13000
	s_add_i32 s87, s75, 0x15000
	s_add_i32 s88, s75, 0x16000
	s_add_i32 s89, s75, 0x18000
	s_add_i32 s90, s75, 0x1a000
	s_add_i32 s91, s75, 0x1c000
	v_lshl_add_u64 v[118:119], v[118:119], 1, s[8:9]
	v_lshl_add_u64 v[120:121], v[120:121], 1, s[8:9]
	v_lshl_add_u64 v[122:123], v[122:123], 1, s[8:9]
	v_lshl_add_u64 v[124:125], v[124:125], 1, s[8:9]
	v_add_u32_e32 v234, v142, v143
	v_add_u32_e32 v235, v144, v143
	v_add_u32_e32 v145, v140, v141
	v_add_u32_e32 v236, v142, v145
	v_add_u32_e32 v237, v144, v145
	v_add_u32_e32 v140, 0xf000, v234
	v_add_u32_e32 v141, 0xf000, v235
	v_add_u32_e32 v142, 0xf000, v236
	v_add_u32_e32 v143, 0xf000, v237
	s_lshr_b32 s93, s11, 1
	s_sub_i32 s93, s93, 1
	s_mov_b32 m0, s84
	s_nop 0
	global_load_lds_dwordx4 v[126:127], off nt
	v_lshl_add_u64 v[126:127], v[126:127], 0, s[0:1]
	s_mov_b32 m0, s85
	s_nop 0
	global_load_lds_dwordx4 v[128:129], off nt
	v_lshl_add_u64 v[128:129], v[128:129], 0, s[0:1]
	s_mov_b32 m0, s86
	s_nop 0
	global_load_lds_dwordx4 v[130:131], off nt
	v_lshl_add_u64 v[130:131], v[130:131], 0, s[0:1]
	s_mov_b32 m0, s87
	s_nop 0
	s_cmp_eq_u32 s92, 0
	s_cbranch_scc1 .Lgp_skip_1
	global_load_lds_dwordx4 v[132:133], off nt
.Lgp_skip_1:
	v_lshl_add_u64 v[132:133], v[132:133], 0, s[0:1]
	s_mov_b32 m0, s88
	s_nop 0
	global_load_lds_dwordx4 v[118:119], off
	v_lshl_add_u64 v[118:119], v[118:119], 0, s[72:73]
	s_mov_b32 m0, s89
	s_nop 0
	global_load_lds_dwordx4 v[120:121], off
	v_lshl_add_u64 v[120:121], v[120:121], 0, s[72:73]
	s_mov_b32 m0, s90
	s_nop 0
	global_load_lds_dwordx4 v[122:123], off
	v_lshl_add_u64 v[122:123], v[122:123], 0, s[72:73]
	s_mov_b32 m0, s91
	s_nop 0
	global_load_lds_dwordx4 v[124:125], off
	v_lshl_add_u64 v[124:125], v[124:125], 0, s[72:73]
	s_cmp_eq_u32 s92, 0
	s_cbranch_scc1 .Lgp_w7
	s_waitcnt vmcnt(8)
	s_branch .Lgp_wj
.Lgp_w7:
	s_waitcnt vmcnt(7)
.Lgp_wj:
	s_barrier
	ds_read_b128 v[178:181], v236 offset:28672
	ds_read_b128 v[186:189], v236 offset:30720
	ds_read_b128 v[174:177], v236 offset:32768
	ds_read_b128 v[182:185], v236 offset:34816
	ds_read_b128 v[146:149], v234
	ds_read_b128 v[150:153], v234 offset:2048
	ds_read_b128 v[154:157], v234 offset:4096
	ds_read_b128 v[158:161], v234 offset:6144
	ds_read_b128 v[162:165], v234 offset:8192
	ds_read_b128 v[166:169], v234 offset:10240
	ds_read_b128 v[170:173], v234 offset:12288
	ds_read_b128 v[218:221], v237 offset:28672
	ds_read_b128 v[222:225], v237 offset:30720
	ds_read_b128 v[226:229], v237 offset:32768
	ds_read_b128 v[230:233], v237 offset:34816
	ds_read_b128 v[190:193], v235
	ds_read_b128 v[194:197], v235 offset:2048
	ds_read_b128 v[198:201], v235 offset:4096
	ds_read_b128 v[202:205], v235 offset:6144
	ds_read_b128 v[206:209], v235 offset:8192
	ds_read_b128 v[210:213], v235 offset:10240
	ds_read_b128 v[214:217], v235 offset:12288
	s_waitcnt lgkmcnt(11)
	v_mfma_f32_16x16x32_f16 v[110:113], v[146:149], v[178:181], v[110:113]
	v_mfma_f32_16x16x32_f16 v[106:109], v[146:149], v[186:189], v[106:109]
	v_mfma_f32_16x16x32_f16 v[50:53], v[146:149], v[174:177], v[50:53]
	v_mfma_f32_16x16x32_f16 v[54:57], v[146:149], v[182:185], v[54:57]
	v_mfma_f32_16x16x32_f16 v[98:101], v[150:153], v[178:181], v[98:101]
	v_mfma_f32_16x16x32_f16 v[102:105], v[150:153], v[186:189], v[102:105]
	v_mfma_f32_16x16x32_f16 v[42:45], v[150:153], v[174:177], v[42:45]
	v_mfma_f32_16x16x32_f16 v[46:49], v[150:153], v[182:185], v[46:49]
	v_mfma_f32_16x16x32_f16 v[90:93], v[154:157], v[178:181], v[90:93]
	v_mfma_f32_16x16x32_f16 v[94:97], v[154:157], v[186:189], v[94:97]
	v_mfma_f32_16x16x32_f16 v[34:37], v[154:157], v[174:177], v[34:37]
	v_mfma_f32_16x16x32_f16 v[38:41], v[154:157], v[182:185], v[38:41]
	v_mfma_f32_16x16x32_f16 v[82:85], v[158:161], v[178:181], v[82:85]
	v_mfma_f32_16x16x32_f16 v[86:89], v[158:161], v[186:189], v[86:89]
	v_mfma_f32_16x16x32_f16 v[18:21], v[158:161], v[174:177], v[18:21]
	v_mfma_f32_16x16x32_f16 v[22:25], v[158:161], v[182:185], v[22:25]
	v_mfma_f32_16x16x32_f16 v[74:77], v[162:165], v[178:181], v[74:77]
	v_mfma_f32_16x16x32_f16 v[78:81], v[162:165], v[186:189], v[78:81]
	v_mfma_f32_16x16x32_f16 v[10:13], v[162:165], v[174:177], v[10:13]
	v_mfma_f32_16x16x32_f16 v[14:17], v[162:165], v[182:185], v[14:17]
	v_mfma_f32_16x16x32_f16 v[66:69], v[166:169], v[178:181], v[66:69]
	v_mfma_f32_16x16x32_f16 v[70:73], v[166:169], v[186:189], v[70:73]
	v_mfma_f32_16x16x32_f16 v[2:5], v[166:169], v[174:177], v[2:5]
	v_mfma_f32_16x16x32_f16 v[6:9], v[166:169], v[182:185], v[6:9]
	v_mfma_f32_16x16x32_f16 v[58:61], v[170:173], v[178:181], v[58:61]
	v_mfma_f32_16x16x32_f16 v[62:65], v[170:173], v[186:189], v[62:65]
	v_mfma_f32_16x16x32_f16 v[26:29], v[170:173], v[174:177], v[26:29]
	v_mfma_f32_16x16x32_f16 v[30:33], v[170:173], v[182:185], v[30:33]
	s_waitcnt lgkmcnt(0)
	s_waitcnt vmcnt(0)
	s_barrier
	.p2alignl 6, 3212836864
.Lgp_loop:
	v_mfma_f32_16x16x32_f16 v[110:113], v[190:193], v[218:221], v[110:113]
	s_mov_b32 m0, s76
	v_mfma_f32_16x16x32_f16 v[106:109], v[190:193], v[222:225], v[106:109]
	global_load_lds_dwordx4 v[126:127], off nt
	v_lshl_add_u64 v[126:127], v[126:127], 0, s[0:1]
	v_mfma_f32_16x16x32_f16 v[50:53], v[190:193], v[226:229], v[50:53]
	s_mov_b32 m0, s77
	v_mfma_f32_16x16x32_f16 v[54:57], v[190:193], v[230:233], v[54:57]
	global_load_lds_dwordx4 v[128:129], off nt
	v_lshl_add_u64 v[128:129], v[128:129], 0, s[0:1]
	v_mfma_f32_16x16x32_f16 v[98:101], v[194:197], v[218:221], v[98:101]
	s_mov_b32 m0, s78
	v_mfma_f32_16x16x32_f16 v[102:105], v[194:197], v[222:225], v[102:105]
	global_load_lds_dwordx4 v[130:131], off nt
	v_lshl_add_u64 v[130:131], v[130:131], 0, s[0:1]
	v_mfma_f32_16x16x32_f16 v[42:45], v[194:197], v[226:229], v[42:45]
	s_mov_b32 m0, s79
	v_mfma_f32_16x16x32_f16 v[46:49], v[194:197], v[230:233], v[46:49]
	s_cmp_eq_u32 s92, 0
	s_cbranch_scc1 .Lgp_skip_2
	global_load_lds_dwordx4 v[132:133], off nt
.Lgp_skip_2:
	v_lshl_add_u64 v[132:133], v[132:133], 0, s[0:1]
	v_mfma_f32_16x16x32_f16 v[90:93], v[198:201], v[218:221], v[90:93]
	s_mov_b32 m0, s80
	v_mfma_f32_16x16x32_f16 v[94:97], v[198:201], v[222:225], v[94:97]
	global_load_lds_dwordx4 v[118:119], off
	v_lshl_add_u64 v[118:119], v[118:119], 0, s[72:73]
	v_mfma_f32_16x16x32_f16 v[34:37], v[198:201], v[226:229], v[34:37]
	s_mov_b32 m0, s81
	v_mfma_f32_16x16x32_f16 v[38:41], v[198:201], v[230:233], v[38:41]
	global_load_lds_dwordx4 v[120:121], off
	v_lshl_add_u64 v[120:121], v[120:121], 0, s[72:73]
	v_mfma_f32_16x16x32_f16 v[82:85], v[202:205], v[218:221], v[82:85]
	s_mov_b32 m0, s82
	v_mfma_f32_16x16x32_f16 v[86:89], v[202:205], v[222:225], v[86:89]
	global_load_lds_dwordx4 v[122:123], off
	v_lshl_add_u64 v[122:123], v[122:123], 0, s[72:73]
	v_mfma_f32_16x16x32_f16 v[18:21], v[202:205], v[226:229], v[18:21]
	s_mov_b32 m0, s83
	v_mfma_f32_16x16x32_f16 v[22:25], v[202:205], v[230:233], v[22:25]
	global_load_lds_dwordx4 v[124:125], off
	v_lshl_add_u64 v[124:125], v[124:125], 0, s[72:73]
	v_mfma_f32_16x16x32_f16 v[74:77], v[206:209], v[218:221], v[74:77]
	ds_read_b128 v[178:181], v142 offset:28672
	v_mfma_f32_16x16x32_f16 v[78:81], v[206:209], v[222:225], v[78:81]
	ds_read_b128 v[186:189], v142 offset:30720
	v_mfma_f32_16x16x32_f16 v[10:13], v[206:209], v[226:229], v[10:13]
	ds_read_b128 v[174:177], v142 offset:32768
	v_mfma_f32_16x16x32_f16 v[14:17], v[206:209], v[230:233], v[14:17]
	ds_read_b128 v[182:185], v142 offset:34816
	v_mfma_f32_16x16x32_f16 v[66:69], v[210:213], v[218:221], v[66:69]
	ds_read_b128 v[146:149], v140
	v_mfma_f32_16x16x32_f16 v[70:73], v[210:213], v[222:225], v[70:73]
	ds_read_b128 v[150:153], v140 offset:2048
	v_mfma_f32_16x16x32_f16 v[2:5], v[210:213], v[226:229], v[2:5]
	ds_read_b128 v[154:157], v140 offset:4096
	v_mfma_f32_16x16x32_f16 v[6:9], v[210:213], v[230:233], v[6:9]
	ds_read_b128 v[158:161], v140 offset:6144
	v_mfma_f32_16x16x32_f16 v[58:61], v[214:217], v[218:221], v[58:61]
	ds_read_b128 v[162:165], v140 offset:8192
	v_mfma_f32_16x16x32_f16 v[62:65], v[214:217], v[222:225], v[62:65]
	ds_read_b128 v[166:169], v140 offset:10240
	v_mfma_f32_16x16x32_f16 v[26:29], v[214:217], v[226:229], v[26:29]
	ds_read_b128 v[170:173], v140 offset:12288
	v_mfma_f32_16x16x32_f16 v[30:33], v[214:217], v[230:233], v[30:33]
	s_waitcnt lgkmcnt(0)
	v_mfma_f32_16x16x32_f16 v[110:113], v[146:149], v[178:181], v[110:113]
	ds_read_b128 v[218:221], v143 offset:28672
	v_mfma_f32_16x16x32_f16 v[106:109], v[146:149], v[186:189], v[106:109]
	ds_read_b128 v[222:225], v143 offset:30720
	v_mfma_f32_16x16x32_f16 v[50:53], v[146:149], v[174:177], v[50:53]
	ds_read_b128 v[226:229], v143 offset:32768
	v_mfma_f32_16x16x32_f16 v[54:57], v[146:149], v[182:185], v[54:57]
	ds_read_b128 v[230:233], v143 offset:34816
	v_mfma_f32_16x16x32_f16 v[98:101], v[150:153], v[178:181], v[98:101]
	ds_read_b128 v[190:193], v141
	v_mfma_f32_16x16x32_f16 v[102:105], v[150:153], v[186:189], v[102:105]
	ds_read_b128 v[194:197], v141 offset:2048
	v_mfma_f32_16x16x32_f16 v[42:45], v[150:153], v[174:177], v[42:45]
	ds_read_b128 v[198:201], v141 offset:4096
	v_mfma_f32_16x16x32_f16 v[46:49], v[150:153], v[182:185], v[46:49]
	ds_read_b128 v[202:205], v141 offset:6144
	v_mfma_f32_16x16x32_f16 v[90:93], v[154:157], v[178:181], v[90:93]
	ds_read_b128 v[206:209], v141 offset:8192
	v_mfma_f32_16x16x32_f16 v[94:97], v[154:157], v[186:189], v[94:97]
	ds_read_b128 v[210:213], v141 offset:10240
	v_mfma_f32_16x16x32_f16 v[34:37], v[154:157], v[174:177], v[34:37]
	ds_read_b128 v[214:217], v141 offset:12288
	v_mfma_f32_16x16x32_f16 v[38:41], v[154:157], v[182:185], v[38:41]
	v_mfma_f32_16x16x32_f16 v[82:85], v[158:161], v[178:181], v[82:85]
	v_mfma_f32_16x16x32_f16 v[86:89], v[158:161], v[186:189], v[86:89]
	v_mfma_f32_16x16x32_f16 v[18:21], v[158:161], v[174:177], v[18:21]
	v_mfma_f32_16x16x32_f16 v[22:25], v[158:161], v[182:185], v[22:25]
	v_mfma_f32_16x16x32_f16 v[74:77], v[162:165], v[178:181], v[74:77]
	v_mfma_f32_16x16x32_f16 v[78:81], v[162:165], v[186:189], v[78:81]
	v_mfma_f32_16x16x32_f16 v[10:13], v[162:165], v[174:177], v[10:13]
	v_mfma_f32_16x16x32_f16 v[14:17], v[162:165], v[182:185], v[14:17]
	v_mfma_f32_16x16x32_f16 v[66:69], v[166:169], v[178:181], v[66:69]
	v_mfma_f32_16x16x32_f16 v[70:73], v[166:169], v[186:189], v[70:73]
	v_mfma_f32_16x16x32_f16 v[2:5], v[166:169], v[174:177], v[2:5]
	v_mfma_f32_16x16x32_f16 v[6:9], v[166:169], v[182:185], v[6:9]
	v_mfma_f32_16x16x32_f16 v[58:61], v[170:173], v[178:181], v[58:61]
	v_mfma_f32_16x16x32_f16 v[62:65], v[170:173], v[186:189], v[62:65]
	v_mfma_f32_16x16x32_f16 v[26:29], v[170:173], v[174:177], v[26:29]
	v_mfma_f32_16x16x32_f16 v[30:33], v[170:173], v[182:185], v[30:33]
	s_waitcnt lgkmcnt(0)
	s_waitcnt vmcnt(0)
	s_barrier
	v_mfma_f32_16x16x32_f16 v[110:113], v[190:193], v[218:221], v[110:113]
	s_mov_b32 m0, s84
	v_mfma_f32_16x16x32_f16 v[106:109], v[190:193], v[222:225], v[106:109]
	global_load_lds_dwordx4 v[126:127], off nt
	v_lshl_add_u64 v[126:127], v[126:127], 0, s[0:1]
	v_mfma_f32_16x16x32_f16 v[50:53], v[190:193], v[226:229], v[50:53]
	s_mov_b32 m0, s85
	v_mfma_f32_16x16x32_f16 v[54:57], v[190:193], v[230:233], v[54:57]
	global_load_lds_dwordx4 v[128:129], off nt
	v_lshl_add_u64 v[128:129], v[128:129], 0, s[0:1]
	v_mfma_f32_16x16x32_f16 v[98:101], v[194:197], v[218:221], v[98:101]
	s_mov_b32 m0, s86
	v_mfma_f32_16x16x32_f16 v[102:105], v[194:197], v[222:225], v[102:105]
	global_load_lds_dwordx4 v[130:131], off nt
	v_lshl_add_u64 v[130:131], v[130:131], 0, s[0:1]
	v_mfma_f32_16x16x32_f16 v[42:45], v[194:197], v[226:229], v[42:45]
	s_mov_b32 m0, s87
	v_mfma_f32_16x16x32_f16 v[46:49], v[194:197], v[230:233], v[46:49]
	s_cmp_eq_u32 s92, 0
	s_cbranch_scc1 .Lgp_skip_3
	global_load_lds_dwordx4 v[132:133], off nt
.Lgp_skip_3:
	v_lshl_add_u64 v[132:133], v[132:133], 0, s[0:1]
	v_mfma_f32_16x16x32_f16 v[90:93], v[198:201], v[218:221], v[90:93]
	s_mov_b32 m0, s88
	v_mfma_f32_16x16x32_f16 v[94:97], v[198:201], v[222:225], v[94:97]
	global_load_lds_dwordx4 v[118:119], off
	v_lshl_add_u64 v[118:119], v[118:119], 0, s[72:73]
	v_mfma_f32_16x16x32_f16 v[34:37], v[198:201], v[226:229], v[34:37]
	s_mov_b32 m0, s89
	v_mfma_f32_16x16x32_f16 v[38:41], v[198:201], v[230:233], v[38:41]
	global_load_lds_dwordx4 v[120:121], off
	v_lshl_add_u64 v[120:121], v[120:121], 0, s[72:73]
	v_mfma_f32_16x16x32_f16 v[82:85], v[202:205], v[218:221], v[82:85]
	s_mov_b32 m0, s90
	v_mfma_f32_16x16x32_f16 v[86:89], v[202:205], v[222:225], v[86:89]
	global_load_lds_dwordx4 v[122:123], off
	v_lshl_add_u64 v[122:123], v[122:123], 0, s[72:73]
	v_mfma_f32_16x16x32_f16 v[18:21], v[202:205], v[226:229], v[18:21]
	s_mov_b32 m0, s91
	v_mfma_f32_16x16x32_f16 v[22:25], v[202:205], v[230:233], v[22:25]
	global_load_lds_dwordx4 v[124:125], off
	v_lshl_add_u64 v[124:125], v[124:125], 0, s[72:73]
	v_mfma_f32_16x16x32_f16 v[74:77], v[206:209], v[218:221], v[74:77]
	ds_read_b128 v[178:181], v236 offset:28672
	v_mfma_f32_16x16x32_f16 v[78:81], v[206:209], v[222:225], v[78:81]
	ds_read_b128 v[186:189], v236 offset:30720
	v_mfma_f32_16x16x32_f16 v[10:13], v[206:209], v[226:229], v[10:13]
	ds_read_b128 v[174:177], v236 offset:32768
	v_mfma_f32_16x16x32_f16 v[14:17], v[206:209], v[230:233], v[14:17]
	ds_read_b128 v[182:185], v236 offset:34816
	v_mfma_f32_16x16x32_f16 v[66:69], v[210:213], v[218:221], v[66:69]
	ds_read_b128 v[146:149], v234
	v_mfma_f32_16x16x32_f16 v[70:73], v[210:213], v[222:225], v[70:73]
	ds_read_b128 v[150:153], v234 offset:2048
	v_mfma_f32_16x16x32_f16 v[2:5], v[210:213], v[226:229], v[2:5]
	ds_read_b128 v[154:157], v234 offset:4096
	v_mfma_f32_16x16x32_f16 v[6:9], v[210:213], v[230:233], v[6:9]
	ds_read_b128 v[158:161], v234 offset:6144
	v_mfma_f32_16x16x32_f16 v[58:61], v[214:217], v[218:221], v[58:61]
	ds_read_b128 v[162:165], v234 offset:8192
	v_mfma_f32_16x16x32_f16 v[62:65], v[214:217], v[222:225], v[62:65]
	ds_read_b128 v[166:169], v234 offset:10240
	v_mfma_f32_16x16x32_f16 v[26:29], v[214:217], v[226:229], v[26:29]
	ds_read_b128 v[170:173], v234 offset:12288
	v_mfma_f32_16x16x32_f16 v[30:33], v[214:217], v[230:233], v[30:33]
	s_waitcnt lgkmcnt(0)
	v_mfma_f32_16x16x32_f16 v[110:113], v[146:149], v[178:181], v[110:113]
	ds_read_b128 v[218:221], v237 offset:28672
	v_mfma_f32_16x16x32_f16 v[106:109], v[146:149], v[186:189], v[106:109]
	ds_read_b128 v[222:225], v237 offset:30720
	v_mfma_f32_16x16x32_f16 v[50:53], v[146:149], v[174:177], v[50:53]
	ds_read_b128 v[226:229], v237 offset:32768
	v_mfma_f32_16x16x32_f16 v[54:57], v[146:149], v[182:185], v[54:57]
	ds_read_b128 v[230:233], v237 offset:34816
	v_mfma_f32_16x16x32_f16 v[98:101], v[150:153], v[178:181], v[98:101]
	ds_read_b128 v[190:193], v235
	v_mfma_f32_16x16x32_f16 v[102:105], v[150:153], v[186:189], v[102:105]
	ds_read_b128 v[194:197], v235 offset:2048
	v_mfma_f32_16x16x32_f16 v[42:45], v[150:153], v[174:177], v[42:45]
	ds_read_b128 v[198:201], v235 offset:4096
	v_mfma_f32_16x16x32_f16 v[46:49], v[150:153], v[182:185], v[46:49]
	ds_read_b128 v[202:205], v235 offset:6144
	v_mfma_f32_16x16x32_f16 v[90:93], v[154:157], v[178:181], v[90:93]
	ds_read_b128 v[206:209], v235 offset:8192
	v_mfma_f32_16x16x32_f16 v[94:97], v[154:157], v[186:189], v[94:97]
	ds_read_b128 v[210:213], v235 offset:10240
	v_mfma_f32_16x16x32_f16 v[34:37], v[154:157], v[174:177], v[34:37]
	ds_read_b128 v[214:217], v235 offset:12288
	v_mfma_f32_16x16x32_f16 v[38:41], v[154:157], v[182:185], v[38:41]
	v_mfma_f32_16x16x32_f16 v[82:85], v[158:161], v[178:181], v[82:85]
	v_mfma_f32_16x16x32_f16 v[86:89], v[158:161], v[186:189], v[86:89]
	v_mfma_f32_16x16x32_f16 v[18:21], v[158:161], v[174:177], v[18:21]
	v_mfma_f32_16x16x32_f16 v[22:25], v[158:161], v[182:185], v[22:25]
	v_mfma_f32_16x16x32_f16 v[74:77], v[162:165], v[178:181], v[74:77]
	v_mfma_f32_16x16x32_f16 v[78:81], v[162:165], v[186:189], v[78:81]
	v_mfma_f32_16x16x32_f16 v[10:13], v[162:165], v[174:177], v[10:13]
	v_mfma_f32_16x16x32_f16 v[14:17], v[162:165], v[182:185], v[14:17]
	v_mfma_f32_16x16x32_f16 v[66:69], v[166:169], v[178:181], v[66:69]
	v_mfma_f32_16x16x32_f16 v[70:73], v[166:169], v[186:189], v[70:73]
	v_mfma_f32_16x16x32_f16 v[2:5], v[166:169], v[174:177], v[2:5]
	v_mfma_f32_16x16x32_f16 v[6:9], v[166:169], v[182:185], v[6:9]
	v_mfma_f32_16x16x32_f16 v[58:61], v[170:173], v[178:181], v[58:61]
	v_mfma_f32_16x16x32_f16 v[62:65], v[170:173], v[186:189], v[62:65]
	v_mfma_f32_16x16x32_f16 v[26:29], v[170:173], v[174:177], v[26:29]
	v_mfma_f32_16x16x32_f16 v[30:33], v[170:173], v[182:185], v[30:33]
	s_waitcnt lgkmcnt(0)
	s_waitcnt vmcnt(0)
	s_barrier
	s_sub_i32 s93, s93, 1
	s_cmp_lg_u32 s93, 0
	s_cbranch_scc1 .Lgp_loop
	v_mfma_f32_16x16x32_f16 v[110:113], v[190:193], v[218:221], v[110:113]
	ds_read_b128 v[178:181], v142 offset:28672
	v_mfma_f32_16x16x32_f16 v[106:109], v[190:193], v[222:225], v[106:109]
	ds_read_b128 v[186:189], v142 offset:30720
	v_mfma_f32_16x16x32_f16 v[50:53], v[190:193], v[226:229], v[50:53]
	ds_read_b128 v[174:177], v142 offset:32768
	v_mfma_f32_16x16x32_f16 v[54:57], v[190:193], v[230:233], v[54:57]
	ds_read_b128 v[182:185], v142 offset:34816
	v_mfma_f32_16x16x32_f16 v[98:101], v[194:197], v[218:221], v[98:101]
	ds_read_b128 v[146:149], v140
	v_mfma_f32_16x16x32_f16 v[102:105], v[194:197], v[222:225], v[102:105]
	ds_read_b128 v[150:153], v140 offset:2048
	v_mfma_f32_16x16x32_f16 v[42:45], v[194:197], v[226:229], v[42:45]
	ds_read_b128 v[154:157], v140 offset:4096
	v_mfma_f32_16x16x32_f16 v[46:49], v[194:197], v[230:233], v[46:49]
	ds_read_b128 v[158:161], v140 offset:6144
	v_mfma_f32_16x16x32_f16 v[90:93], v[198:201], v[218:221], v[90:93]
	ds_read_b128 v[162:165], v140 offset:8192
	v_mfma_f32_16x16x32_f16 v[94:97], v[198:201], v[222:225], v[94:97]
	ds_read_b128 v[166:169], v140 offset:10240
	v_mfma_f32_16x16x32_f16 v[34:37], v[198:201], v[226:229], v[34:37]
	ds_read_b128 v[170:173], v140 offset:12288
	v_mfma_f32_16x16x32_f16 v[38:41], v[198:201], v[230:233], v[38:41]
	v_mfma_f32_16x16x32_f16 v[82:85], v[202:205], v[218:221], v[82:85]
	v_mfma_f32_16x16x32_f16 v[86:89], v[202:205], v[222:225], v[86:89]
	v_mfma_f32_16x16x32_f16 v[18:21], v[202:205], v[226:229], v[18:21]
	v_mfma_f32_16x16x32_f16 v[22:25], v[202:205], v[230:233], v[22:25]
	v_mfma_f32_16x16x32_f16 v[74:77], v[206:209], v[218:221], v[74:77]
	v_mfma_f32_16x16x32_f16 v[78:81], v[206:209], v[222:225], v[78:81]
	v_mfma_f32_16x16x32_f16 v[10:13], v[206:209], v[226:229], v[10:13]
	v_mfma_f32_16x16x32_f16 v[14:17], v[206:209], v[230:233], v[14:17]
	v_mfma_f32_16x16x32_f16 v[66:69], v[210:213], v[218:221], v[66:69]
	v_mfma_f32_16x16x32_f16 v[70:73], v[210:213], v[222:225], v[70:73]
	v_mfma_f32_16x16x32_f16 v[2:5], v[210:213], v[226:229], v[2:5]
	v_mfma_f32_16x16x32_f16 v[6:9], v[210:213], v[230:233], v[6:9]
	v_mfma_f32_16x16x32_f16 v[58:61], v[214:217], v[218:221], v[58:61]
	v_mfma_f32_16x16x32_f16 v[62:65], v[214:217], v[222:225], v[62:65]
	v_mfma_f32_16x16x32_f16 v[26:29], v[214:217], v[226:229], v[26:29]
	v_mfma_f32_16x16x32_f16 v[30:33], v[214:217], v[230:233], v[30:33]
	s_waitcnt lgkmcnt(0)
	v_mfma_f32_16x16x32_f16 v[110:113], v[146:149], v[178:181], v[110:113]
	ds_read_b128 v[218:221], v143 offset:28672
	v_mfma_f32_16x16x32_f16 v[106:109], v[146:149], v[186:189], v[106:109]
	ds_read_b128 v[222:225], v143 offset:30720
	v_mfma_f32_16x16x32_f16 v[50:53], v[146:149], v[174:177], v[50:53]
	ds_read_b128 v[226:229], v143 offset:32768
	v_mfma_f32_16x16x32_f16 v[54:57], v[146:149], v[182:185], v[54:57]
	ds_read_b128 v[230:233], v143 offset:34816
	v_mfma_f32_16x16x32_f16 v[98:101], v[150:153], v[178:181], v[98:101]
	ds_read_b128 v[190:193], v141
	v_mfma_f32_16x16x32_f16 v[102:105], v[150:153], v[186:189], v[102:105]
	ds_read_b128 v[194:197], v141 offset:2048
	v_mfma_f32_16x16x32_f16 v[42:45], v[150:153], v[174:177], v[42:45]
	ds_read_b128 v[198:201], v141 offset:4096
	v_mfma_f32_16x16x32_f16 v[46:49], v[150:153], v[182:185], v[46:49]
	ds_read_b128 v[202:205], v141 offset:6144
	v_mfma_f32_16x16x32_f16 v[90:93], v[154:157], v[178:181], v[90:93]
	ds_read_b128 v[206:209], v141 offset:8192
	v_mfma_f32_16x16x32_f16 v[94:97], v[154:157], v[186:189], v[94:97]
	ds_read_b128 v[210:213], v141 offset:10240
	v_mfma_f32_16x16x32_f16 v[34:37], v[154:157], v[174:177], v[34:37]
	ds_read_b128 v[214:217], v141 offset:12288
	v_mfma_f32_16x16x32_f16 v[38:41], v[154:157], v[182:185], v[38:41]
	v_mfma_f32_16x16x32_f16 v[82:85], v[158:161], v[178:181], v[82:85]
	v_mfma_f32_16x16x32_f16 v[86:89], v[158:161], v[186:189], v[86:89]
	v_mfma_f32_16x16x32_f16 v[18:21], v[158:161], v[174:177], v[18:21]
	v_mfma_f32_16x16x32_f16 v[22:25], v[158:161], v[182:185], v[22:25]
	v_mfma_f32_16x16x32_f16 v[74:77], v[162:165], v[178:181], v[74:77]
	v_mfma_f32_16x16x32_f16 v[78:81], v[162:165], v[186:189], v[78:81]
	v_mfma_f32_16x16x32_f16 v[10:13], v[162:165], v[174:177], v[10:13]
	v_mfma_f32_16x16x32_f16 v[14:17], v[162:165], v[182:185], v[14:17]
	v_mfma_f32_16x16x32_f16 v[66:69], v[166:169], v[178:181], v[66:69]
	v_mfma_f32_16x16x32_f16 v[70:73], v[166:169], v[186:189], v[70:73]
	v_mfma_f32_16x16x32_f16 v[2:5], v[166:169], v[174:177], v[2:5]
	v_mfma_f32_16x16x32_f16 v[6:9], v[166:169], v[182:185], v[6:9]
	v_mfma_f32_16x16x32_f16 v[58:61], v[170:173], v[178:181], v[58:61]
	v_mfma_f32_16x16x32_f16 v[62:65], v[170:173], v[186:189], v[62:65]
	v_mfma_f32_16x16x32_f16 v[26:29], v[170:173], v[174:177], v[26:29]
	v_mfma_f32_16x16x32_f16 v[30:33], v[170:173], v[182:185], v[30:33]
	s_waitcnt lgkmcnt(0)
	v_mfma_f32_16x16x32_f16 v[110:113], v[190:193], v[218:221], v[110:113]
	v_mfma_f32_16x16x32_f16 v[106:109], v[190:193], v[222:225], v[106:109]
	v_mfma_f32_16x16x32_f16 v[50:53], v[190:193], v[226:229], v[50:53]
	v_mfma_f32_16x16x32_f16 v[54:57], v[190:193], v[230:233], v[54:57]
	v_mfma_f32_16x16x32_f16 v[98:101], v[194:197], v[218:221], v[98:101]
	v_mfma_f32_16x16x32_f16 v[102:105], v[194:197], v[222:225], v[102:105]
	v_mfma_f32_16x16x32_f16 v[42:45], v[194:197], v[226:229], v[42:45]
	v_mfma_f32_16x16x32_f16 v[46:49], v[194:197], v[230:233], v[46:49]
	v_mfma_f32_16x16x32_f16 v[90:93], v[198:201], v[218:221], v[90:93]
	v_mfma_f32_16x16x32_f16 v[94:97], v[198:201], v[222:225], v[94:97]
	v_mfma_f32_16x16x32_f16 v[34:37], v[198:201], v[226:229], v[34:37]
	v_mfma_f32_16x16x32_f16 v[38:41], v[198:201], v[230:233], v[38:41]
	v_mfma_f32_16x16x32_f16 v[82:85], v[202:205], v[218:221], v[82:85]
	v_mfma_f32_16x16x32_f16 v[86:89], v[202:205], v[222:225], v[86:89]
	v_mfma_f32_16x16x32_f16 v[18:21], v[202:205], v[226:229], v[18:21]
	v_mfma_f32_16x16x32_f16 v[22:25], v[202:205], v[230:233], v[22:25]
	v_mfma_f32_16x16x32_f16 v[74:77], v[206:209], v[218:221], v[74:77]
	v_mfma_f32_16x16x32_f16 v[78:81], v[206:209], v[222:225], v[78:81]
	v_mfma_f32_16x16x32_f16 v[10:13], v[206:209], v[226:229], v[10:13]
	v_mfma_f32_16x16x32_f16 v[14:17], v[206:209], v[230:233], v[14:17]
	v_mfma_f32_16x16x32_f16 v[66:69], v[210:213], v[218:221], v[66:69]
	v_mfma_f32_16x16x32_f16 v[70:73], v[210:213], v[222:225], v[70:73]
	v_mfma_f32_16x16x32_f16 v[2:5], v[210:213], v[226:229], v[2:5]
	v_mfma_f32_16x16x32_f16 v[6:9], v[210:213], v[230:233], v[6:9]
	v_mfma_f32_16x16x32_f16 v[58:61], v[214:217], v[218:221], v[58:61]
	v_mfma_f32_16x16x32_f16 v[62:65], v[214:217], v[222:225], v[62:65]
	v_mfma_f32_16x16x32_f16 v[26:29], v[214:217], v[226:229], v[26:29]
	v_mfma_f32_16x16x32_f16 v[30:33], v[214:217], v[230:233], v[30:33]

.LBB5_18:
	s_or_b64 exec, exec, s[0:1]
	s_waitcnt lgkmcnt(7)
	v_lshrrev_b32_e32 v3, 5, v0
	v_and_b32_e32 v1, 31, v0
	v_lshrrev_b32_e32 v2, 7, v0
	v_or_b32_e32 v4, s3, v3
	s_mov_b32 s8, 0xc350
	v_bitop3_b32 v2, v2, v1, 2 bitop3:0x6c
	v_cmp_gt_i32_e32 vcc, s8, v4
	s_mov_b32 s7, 0x20000
	s_mov_b32 s6, 0x186a000
	s_and_b32 s5, s59, 0xffff
	v_lshl_add_u32 v2, v2, 4, 0
	v_lshlrev_b32_e32 v1, 4, v1
	s_or_b64 s[10:11], s[66:67], vcc
	s_waitcnt lgkmcnt(0)
	s_barrier
	s_movk_i32 s4, 0x210
	v_mad_u32_u24 v5, v3, s4, v2
	v_add_u32_e32 v10, 0x10800, v5
	v_lshl_or_b32 v4, v4, 9, v1
	s_mov_b32 s4, s58
	ds_read_b128 v[12:15], v5
	ds_read_b128 v[16:19], v5 offset:8448
	ds_read_b128 v[20:23], v5 offset:16896
	ds_read_b128 v[24:27], v5 offset:25344
	ds_read_b128 v[28:31], v5 offset:33792
	ds_read_b128 v[32:35], v5 offset:42240
	ds_read_b128 v[36:39], v5 offset:50688
	ds_read_b128 v[40:43], v5 offset:59136
	ds_read_b128 v[44:47], v10
	ds_read_b128 v[48:51], v10 offset:8448
	ds_read_b128 v[52:55], v10 offset:16896
	ds_read_b128 v[56:59], v10 offset:25344
	ds_read_b128 v[60:63], v10 offset:33792
	ds_read_b128 v[64:67], v10 offset:42240
	s_waitcnt lgkmcnt(13)
	buffer_store_dwordx4 v[12:15], v4, s[4:7], 0 offen sc1
	s_waitcnt lgkmcnt(12)
	s_mov_b32 s8, 0x2000
	buffer_store_dwordx4 v[16:19], v4, s[4:7], s8 offen sc1
	s_waitcnt lgkmcnt(11)
	s_mov_b32 s8, 0x4000
	buffer_store_dwordx4 v[20:23], v4, s[4:7], s8 offen sc1
	s_waitcnt lgkmcnt(10)
	s_mov_b32 s8, 0x6000
	buffer_store_dwordx4 v[24:27], v4, s[4:7], s8 offen sc1
	s_waitcnt lgkmcnt(9)
	s_mov_b32 s8, 0x8000
	buffer_store_dwordx4 v[28:31], v4, s[4:7], s8 offen sc1
	s_waitcnt lgkmcnt(8)
	s_mov_b32 s8, 0xa000
	buffer_store_dwordx4 v[32:35], v4, s[4:7], s8 offen sc1
	s_waitcnt lgkmcnt(7)
	s_mov_b32 s8, 0xc000
	buffer_store_dwordx4 v[36:39], v4, s[4:7], s8 offen sc1
	s_waitcnt lgkmcnt(6)
	s_mov_b32 s8, 0xe000
	buffer_store_dwordx4 v[40:43], v4, s[4:7], s8 offen sc1
	s_waitcnt lgkmcnt(5)
	s_mov_b32 s8, 0x10000
	buffer_store_dwordx4 v[44:47], v4, s[4:7], s8 offen sc1
	s_waitcnt lgkmcnt(4)
	s_mov_b32 s8, 0x12000
	buffer_store_dwordx4 v[48:51], v4, s[4:7], s8 offen sc1
	s_waitcnt lgkmcnt(3)
	s_mov_b32 s8, 0x14000
	buffer_store_dwordx4 v[52:55], v4, s[4:7], s8 offen sc1
	s_waitcnt lgkmcnt(2)
	s_mov_b32 s8, 0x16000
	buffer_store_dwordx4 v[56:59], v4, s[4:7], s8 offen sc1
	s_waitcnt lgkmcnt(1)
	s_mov_b32 s8, 0x18000
	buffer_store_dwordx4 v[60:63], v4, s[4:7], s8 offen sc1
	s_waitcnt lgkmcnt(0)
	s_mov_b32 s8, 0x1a000
	buffer_store_dwordx4 v[64:67], v4, s[4:7], s8 offen sc1
